# speedup vs baseline: 1.0743x; 1.0019x over previous
.LBB1_70:
	s_or_b64 exec, exec, s[4:5]
	v_cmp_gt_u32_e64 s[2:3], 32, v244
	v_mov_b32_e32 v59, 0
	v_mov_b32_e32 v6, 0
	s_waitcnt lgkmcnt(0)
	s_barrier
	s_and_saveexec_b64 s[4:5], s[2:3]
	v_mov_b32_e32 v0, 0x27610
	v_lshl_add_u32 v0, v244, 2, v0
	ds_read_b32 v6, v0
	s_or_b64 exec, exec, s[4:5]
	s_load_dwordx4 s[12:15], s[0:1], 0x8
	s_load_dwordx4 s[16:19], s[0:1], 0x58
	v_lshlrev_b32_e32 v60, 2, v244
	s_cmp_lg_u32 s7, 0
	v_add_u32_e32 v0, 0x27690, v60
	v_lshlrev_b32_e32 v58, 4, v174
	s_cselect_b64 s[28:29], -1, 0
	s_cmp_lg_u32 s6, 0
	v_accvgpr_write_b32 a143, v0
	s_waitcnt lgkmcnt(0)
	v_lshl_add_u64 v[0:1], s[12:13], 0, v[58:59]
	s_mov_b64 s[6:7], 0x60000
	v_lshl_add_u64 v[0:1], v[0:1], 0, s[6:7]
	v_lshl_add_u64 v[62:63], v[0:1], 0, v[120:121]
	s_mov_b64 s[6:7], 0x6000
	v_lshl_add_u64 v[2:3], v[62:63], 0, s[6:7]
	v_accvgpr_write_b32 a147, v3
	s_mov_b64 s[6:7], 0x6400
	v_accvgpr_write_b32 a146, v2
	v_lshl_add_u64 v[2:3], v[62:63], 0, s[6:7]
	v_accvgpr_write_b32 a149, v3
	s_mov_b64 s[6:7], 0x6800
	v_accvgpr_write_b32 a148, v2
	v_lshl_add_u64 v[2:3], v[62:63], 0, s[6:7]
	v_accvgpr_write_b32 a151, v3
	s_mov_b64 s[6:7], 0x6c00
	v_accvgpr_write_b32 a150, v2
	v_lshl_add_u64 v[2:3], v[62:63], 0, s[6:7]
	s_mov_b64 s[6:7], 0x1000
	v_accvgpr_write_b32 a153, v3
	v_lshl_add_u64 v[222:223], v[62:63], 0, s[6:7]
	s_mov_b64 s[6:7], 0x7000
	v_accvgpr_write_b32 a152, v2
	v_lshl_add_u64 v[2:3], v[62:63], 0, s[6:7]
	s_mov_b64 s[6:7], 0x1400
	v_accvgpr_write_b32 a155, v3
	v_lshl_add_u64 v[76:77], v[62:63], 0, s[6:7]
	s_mov_b64 s[6:7], 0x7400
	v_accvgpr_write_b32 a154, v2
	v_lshl_add_u64 v[2:3], v[62:63], 0, s[6:7]
	v_accvgpr_write_b32 a157, v3
	s_mov_b64 s[6:7], 0x18000
	v_accvgpr_write_b32 a156, v2
	v_lshl_add_u64 v[2:3], v[62:63], 0, s[6:7]
	v_accvgpr_write_b32 a159, v3
	s_mov_b64 s[6:7], 0x18400
	v_accvgpr_write_b32 a158, v2
	v_lshl_add_u64 v[2:3], v[62:63], 0, s[6:7]
	v_accvgpr_write_b32 a161, v3
	s_mov_b64 s[6:7], 0x18800
	v_accvgpr_write_b32 a160, v2
	v_lshl_add_u64 v[2:3], v[62:63], 0, s[6:7]
	v_accvgpr_write_b32 a163, v3
	s_mov_b64 s[6:7], 0x18c00
	v_accvgpr_write_b32 a162, v2
	v_lshl_add_u64 v[2:3], v[62:63], 0, s[6:7]
	v_accvgpr_write_b32 a165, v3
	s_mov_b64 s[6:7], 0x19000
	v_accvgpr_write_b32 a164, v2
	v_lshl_add_u64 v[2:3], v[62:63], 0, s[6:7]
	v_accvgpr_write_b32 a167, v3
	s_mov_b64 s[6:7], 0x19400
	v_accvgpr_write_b32 a166, v2
	v_lshl_add_u64 v[2:3], v[62:63], 0, s[6:7]
	v_accvgpr_write_b32 a169, v3
	v_lshl_add_u64 v[0:1], v[0:1], 0, v[122:123]
	s_mov_b64 s[6:7], 0x48000
	v_accvgpr_write_b32 a168, v2
	v_lshl_add_u64 v[2:3], v[0:1], 0, s[6:7]
	v_accvgpr_write_b32 a171, v3
	s_mov_b64 s[8:9], 0x48400
	v_accvgpr_write_b32 a170, v2
	v_lshl_add_u64 v[2:3], v[0:1], 0, s[8:9]
	v_accvgpr_write_b32 a173, v3
	s_mov_b64 s[8:9], 0x48800
	v_accvgpr_write_b32 a172, v2
	v_lshl_add_u64 v[2:3], v[0:1], 0, s[8:9]
	v_accvgpr_write_b32 a175, v3
	s_mov_b64 s[8:9], 0x48c00
	v_accvgpr_write_b32 a174, v2
	v_lshl_add_u64 v[2:3], v[0:1], 0, s[8:9]
	v_accvgpr_write_b32 a177, v3
	v_accvgpr_write_b32 a176, v2
	v_lshl_add_u64 v[2:3], v[222:223], 0, v[120:121]
	v_lshl_add_u64 v[4:5], v[2:3], 0, s[6:7]
	v_accvgpr_write_b32 a179, v5
	v_accvgpr_write_b32 a178, v4
	v_lshl_add_u64 v[4:5], v[76:77], 0, v[120:121]
	v_lshl_add_u64 v[8:9], v[4:5], 0, s[6:7]
	v_accvgpr_write_b32 a181, v9
	s_mov_b64 s[6:7], 0x49800
	v_accvgpr_write_b32 a180, v8
	v_lshl_add_u64 v[8:9], v[0:1], 0, s[6:7]
	v_accvgpr_write_b32 a183, v9
	s_mov_b64 s[6:7], 0x49c00
	v_accvgpr_write_b32 a182, v8
	v_lshl_add_u64 v[8:9], v[0:1], 0, s[6:7]
	v_accvgpr_write_b32 a185, v9
	s_mov_b64 s[6:7], 0x4a000
	v_accvgpr_write_b32 a184, v8
	v_lshl_add_u64 v[8:9], v[0:1], 0, s[6:7]
	v_accvgpr_write_b32 a187, v9
	s_mov_b64 s[6:7], 0x4a400
	v_accvgpr_write_b32 a186, v8
	v_lshl_add_u64 v[8:9], v[0:1], 0, s[6:7]
	v_accvgpr_write_b32 a189, v9
	s_mov_b64 s[6:7], 0x4a800
	v_accvgpr_write_b32 a188, v8
	v_lshl_add_u64 v[8:9], v[0:1], 0, s[6:7]
	v_accvgpr_write_b32 a191, v9
	s_mov_b64 s[6:7], 0x4ac00
	v_accvgpr_write_b32 a190, v8
	v_lshl_add_u64 v[8:9], v[0:1], 0, s[6:7]
	v_accvgpr_write_b32 a193, v9
	s_mov_b64 s[6:7], 0x30000
	v_accvgpr_write_b32 a192, v8
	v_lshl_add_u64 v[8:9], v[0:1], 0, s[6:7]
	v_accvgpr_write_b32 a195, v9
	s_mov_b64 s[8:9], 0x3c000
	v_accvgpr_write_b32 a194, v8
	v_lshl_add_u64 v[8:9], v[0:1], 0, s[8:9]
	v_accvgpr_write_b32 a197, v9
	s_mov_b64 s[8:9], 0x30400
	v_accvgpr_write_b32 a196, v8
	v_lshl_add_u64 v[8:9], v[0:1], 0, s[8:9]
	v_accvgpr_write_b32 a199, v9
	s_mov_b64 s[8:9], 0x3c400
	v_accvgpr_write_b32 a198, v8
	v_lshl_add_u64 v[8:9], v[0:1], 0, s[8:9]
	v_accvgpr_write_b32 a201, v9
	s_mov_b64 s[8:9], 0x30800
	v_accvgpr_write_b32 a200, v8
	v_lshl_add_u64 v[8:9], v[0:1], 0, s[8:9]
	v_accvgpr_write_b32 a203, v9
	s_mov_b64 s[8:9], 0x3c800
	v_accvgpr_write_b32 a202, v8
	v_lshl_add_u64 v[8:9], v[0:1], 0, s[8:9]
	v_accvgpr_write_b32 a205, v9
	s_mov_b64 s[8:9], 0x30c00
	v_accvgpr_write_b32 a204, v8
	v_lshl_add_u64 v[8:9], v[0:1], 0, s[8:9]
	v_accvgpr_write_b32 a207, v9
	s_mov_b64 s[8:9], 0x3cc00
	v_lshl_add_u64 v[2:3], v[2:3], 0, s[6:7]
	v_accvgpr_write_b32 a206, v8
	v_lshl_add_u64 v[8:9], v[0:1], 0, s[8:9]
	v_accvgpr_write_b32 a211, v3
	s_mov_b64 s[8:9], 0x3d000
	v_accvgpr_write_b32 a210, v2
	v_lshl_add_u64 v[2:3], v[0:1], 0, s[8:9]
	v_accvgpr_write_b32 a213, v3
	v_accvgpr_write_b32 a212, v2
	v_lshl_add_u64 v[2:3], v[4:5], 0, s[6:7]
	v_accvgpr_write_b32 a215, v3
	s_mov_b64 s[6:7], 0x3d400
	v_accvgpr_write_b32 a214, v2
	v_lshl_add_u64 v[2:3], v[0:1], 0, s[6:7]
	v_accvgpr_write_b32 a217, v3
	s_mov_b64 s[6:7], 0x31800
	v_accvgpr_write_b32 a216, v2
	v_lshl_add_u64 v[2:3], v[0:1], 0, s[6:7]
	v_accvgpr_write_b32 a219, v3
	s_mov_b64 s[6:7], 0x3d800
	v_accvgpr_write_b32 a218, v2
	v_lshl_add_u64 v[2:3], v[0:1], 0, s[6:7]
	v_accvgpr_write_b32 a221, v3
	s_mov_b64 s[6:7], 0x31c00
	v_accvgpr_write_b32 a220, v2
	v_lshl_add_u64 v[2:3], v[0:1], 0, s[6:7]
	v_accvgpr_write_b32 a223, v3
	s_mov_b64 s[6:7], 0x3dc00
	v_accvgpr_write_b32 a222, v2
	v_lshl_add_u64 v[2:3], v[0:1], 0, s[6:7]
	v_accvgpr_write_b32 a225, v3
	s_mov_b64 s[6:7], 0x32000
	v_accvgpr_write_b32 a224, v2
	v_lshl_add_u64 v[2:3], v[0:1], 0, s[6:7]
	v_accvgpr_write_b32 a227, v3
	s_mov_b64 s[6:7], 0x3e000
	v_accvgpr_write_b32 a226, v2
	v_lshl_add_u64 v[2:3], v[0:1], 0, s[6:7]
	v_accvgpr_write_b32 a229, v3
	s_mov_b64 s[6:7], 0x32400
	v_accvgpr_write_b32 a228, v2
	v_lshl_add_u64 v[2:3], v[0:1], 0, s[6:7]
	v_accvgpr_write_b32 a231, v3
	s_mov_b64 s[6:7], 0x3e400
	v_accvgpr_write_b32 a230, v2
	v_lshl_add_u64 v[2:3], v[0:1], 0, s[6:7]
	v_accvgpr_write_b32 a233, v3
	s_mov_b64 s[6:7], 0x32800
	v_accvgpr_write_b32 a232, v2
	v_lshl_add_u64 v[2:3], v[0:1], 0, s[6:7]
	v_accvgpr_write_b32 a235, v3
	s_mov_b64 s[6:7], 0x3e800
	v_accvgpr_write_b32 a234, v2
	v_lshl_add_u64 v[2:3], v[0:1], 0, s[6:7]
	s_mov_b64 s[6:7], 0x32c00
	s_mul_hi_u32 s4, s26, 0x13b13b14
	v_lshl_add_u64 v[4:5], v[0:1], 0, s[6:7]
	s_mov_b64 s[6:7], 0x3ec00
	s_mul_i32 s4, s4, 13
	v_lshl_add_u64 v[166:167], v[0:1], 0, s[6:7]
	s_load_dwordx2 s[6:7], s[0:1], 0x70
	s_cselect_b64 s[30:31], -1, 0
	s_sub_i32 s4, s26, s4
	v_lshlrev_b32_e32 v0, 7, v170
	s_add_i32 s5, s4, 1
	s_add_i32 s12, s4, 2
	s_add_i32 s34, s4, 3
	s_add_i32 s37, s4, 4
	s_add_i32 s40, s4, 5
	s_add_i32 s43, s4, 6
	s_add_i32 s46, s4, 7
	s_add_i32 s49, s4, 8
	s_add_i32 s52, s4, 9
	s_add_i32 s55, s4, 10
	s_add_i32 s58, s4, 11
	s_add_i32 s61, s4, 12
	v_lshl_or_b32 v58, s33, 9, v0
	s_lshl_b32 s10, s5, 10
	s_lshl_b32 s13, s12, 10
	s_lshl_b32 s35, s34, 10
	s_lshl_b32 s38, s37, 10
	s_lshl_b32 s41, s40, 10
	s_lshl_b32 s44, s43, 10
	s_lshl_b32 s47, s46, 10
	s_lshl_b32 s50, s49, 10
	s_lshl_b32 s53, s52, 10
	s_lshl_b32 s56, s55, 10
	s_lshl_b32 s59, s58, 10
	s_lshl_b32 s8, s61, 10
	s_mov_b32 s27, 0
	s_lshl_b32 s24, s26, 4
	v_accvgpr_write_b32 a145, v0
	v_lshl_add_u64 v[0:1], s[18:19], 0, v[58:59]
	s_lshl_b32 s18, s4, 10
	s_add_i32 s11, s10, 0xffffcc00
	s_add_i32 s19, s13, 0xffffcc00
	s_add_i32 s36, s35, 0xffffcc00
	s_add_i32 s39, s38, 0xffffcc00
	s_add_i32 s42, s41, 0xffffcc00
	s_add_i32 s45, s44, 0xffffcc00
	s_add_i32 s48, s47, 0xffffcc00
	s_add_i32 s51, s50, 0xffffcc00
	s_add_i32 s54, s53, 0xffffcc00
	s_add_i32 s57, s56, 0xffffcc00
	s_add_i32 s60, s59, 0xffffcc00
	s_add_i32 s62, s8, 0xffffcc00
	s_mul_i32 s8, s33, 0x640
	s_mov_b32 s25, s27
	s_waitcnt lgkmcnt(0)
	s_add_u32 s8, s6, s8
	s_addc_u32 s9, s7, 0
	s_lshl_b64 s[6:7], s[24:25], 2
	s_add_u32 s8, s8, s6
	s_addc_u32 s9, s9, s7
	s_lshl_b32 s5, s5, 6
	s_add_i32 s6, s5, 0xfffffcc0
	s_cmp_gt_u32 s4, 11
	s_cselect_b32 s25, s11, s10
	s_cselect_b32 s10, s6, s5
	s_lshl_b32 s5, s12, 6
	s_add_i32 s6, s5, 0xfffffcc0
	s_cmp_gt_u32 s4, 10
	s_cselect_b32 s19, s19, s13
	s_cselect_b32 s11, s6, s5
	s_lshl_b32 s5, s34, 6
	s_add_i32 s6, s5, 0xfffffcc0
	s_cmp_gt_u32 s4, 9
	s_cselect_b32 s34, s36, s35
	s_cselect_b32 s12, s6, s5
	s_lshl_b32 s5, s37, 6
	s_add_i32 s6, s5, 0xfffffcc0
	s_cmp_gt_u32 s4, 8
	s_cselect_b32 s35, s39, s38
	s_cselect_b32 s13, s6, s5
	s_lshl_b32 s5, s40, 6
	s_add_i32 s6, s5, 0xfffffcc0
	s_cmp_gt_u32 s4, 7
	s_cselect_b32 s36, s42, s41
	s_cselect_b32 s37, s6, s5
	s_lshl_b32 s5, s43, 6
	s_add_i32 s6, s5, 0xfffffcc0
	s_cmp_gt_u32 s4, 6
	s_cselect_b32 s38, s45, s44
	s_cselect_b32 s39, s6, s5
	s_lshl_b32 s5, s46, 6
	s_add_i32 s6, s5, 0xfffffcc0
	s_cmp_gt_u32 s4, 5
	s_cselect_b32 s40, s48, s47
	s_cselect_b32 s41, s6, s5
	s_lshl_b32 s5, s49, 6
	s_add_i32 s6, s5, 0xfffffcc0
	s_cmp_gt_u32 s4, 4
	s_cselect_b32 s42, s51, s50
	s_cselect_b32 s43, s6, s5
	s_lshl_b32 s5, s52, 6
	s_add_i32 s6, s5, 0xfffffcc0
	s_cmp_gt_u32 s4, 3
	s_cselect_b32 s44, s54, s53
	s_cselect_b32 s45, s6, s5
	s_lshl_b32 s5, s55, 6
	s_add_i32 s6, s5, 0xfffffcc0
	s_cmp_gt_u32 s4, 2
	s_cselect_b32 s46, s57, s56
	s_cselect_b32 s47, s6, s5
	s_lshl_b32 s5, s58, 6
	s_add_i32 s6, s5, 0xfffffcc0
	s_cmp_gt_u32 s4, 1
	v_accvgpr_write_b32 a209, v9
	v_accvgpr_write_b32 a237, v3
	s_cselect_b32 s48, s60, s59
	s_cselect_b32 s49, s6, s5
	s_lshl_b32 s5, s61, 6
	v_accvgpr_write_b32 a208, v8
	v_accvgpr_write_b32 a236, v2
	v_min_u32_e32 v2, 24, v174
	v_lshl_or_b32 v8, s33, 2, v170
	s_add_i32 s50, s5, 0xfffffcc0
	v_lshlrev_b32_e32 v58, 2, v2
	v_mul_u32_u24_e32 v2, 0x3400, v8
	s_cmp_eq_u32 s4, 0
	v_or_b32_e32 v2, v2, v180
	s_cselect_b32 s51, 0x3000, s62
	v_mov_b32_e32 v61, v59
	s_waitcnt vmcnt(0)
	v_accvgpr_read_b32 v3, a142
	v_lshlrev_b32_e32 v7, 2, v183
	v_add_u32_e32 v194, s18, v2
	v_add_u32_e32 v195, s25, v2
	v_add_u32_e32 v196, s19, v2
	v_add_u32_e32 v197, s34, v2
	v_add_u32_e32 v198, s35, v2
	v_add_u32_e32 v199, s36, v2
	v_add_u32_e32 v200, s38, v2
	v_add_u32_e32 v201, s40, v2
	v_add_u32_e32 v202, s42, v2
	v_add_u32_e32 v203, s44, v2
	v_add_u32_e32 v204, s46, v2
	v_add_u32_e32 v205, s48, v2
	v_add_u32_e32 v206, s51, v2
	v_lshl_add_u64 v[170:171], s[8:9], 0, v[60:61]
	v_lshl_or_b32 v213, s37, 4, v180
	s_cselect_b32 s8, 0x300, s50
	v_and_b32_e32 v2, 16, v244
	v_mul_f32_e32 v3, v3, v6
	v_or_b32_e32 v6, s24, v181
	v_or_b32_e32 v11, 32, v8
	s_bfe_u32 s37, s26, 0x1b0001
	v_lshl_add_u64 v[168:169], v[0:1], 0, v[58:59]
	v_lshl_or_b32 v2, v2, 2, v7
	v_mad_u32_u24 v58, v11, 13, s37
	v_lshlrev_b32_e32 v6, 1, v6
	v_accvgpr_write_b32 a238, v3
	v_accvgpr_write_b32 a239, v2
	v_lshlrev_b64 v[2:3], 10, v[58:59]
	v_and_or_b32 v6, v6, 48, v183
	v_lshl_add_u64 v[2:3], s[16:17], 0, v[2:3]
	v_lshlrev_b32_e32 v58, 4, v6
	v_and_b32_e32 v6, 4, v111
	v_accvgpr_write_b32 a144, v7
	v_lshl_add_u64 v[2:3], v[2:3], 0, v[58:59]
	v_lshlrev_b32_e32 v6, 1, v6
	v_mov_b32_e32 v7, v59
	s_lshl_b32 s26, s26, 2
	v_lshl_or_b32 v209, s10, 4, v180
	v_lshl_or_b32 v210, s11, 4, v180
	v_lshl_or_b32 v211, s12, 4, v180
	v_lshl_or_b32 v212, s13, 4, v180
	v_cmp_gt_u32_e64 s[10:11], 16, v174
	v_lshl_add_u64 v[172:173], v[2:3], 0, v[6:7]
	v_lshlrev_b32_e32 v2, 1, v175
	v_cmp_eq_u32_e64 s[12:13], 0, v174
	v_lshl_add_u64 v[174:175], v[0:1], 0, s[26:27]
	v_mul_u32_u24_e32 v0, 0x3400, v11
	v_or_b32_e32 v0, v0, v180
	v_add_u32_e32 v229, s18, v0
	v_add_u32_e32 v230, s25, v0
	v_add_u32_e32 v231, s19, v0
	v_add_u32_e32 v232, s34, v0
	v_add_u32_e32 v233, s35, v0
	v_add_u32_e32 v234, s36, v0
	v_add_u32_e32 v235, s38, v0
	v_add_u32_e32 v236, s40, v0
	v_add_u32_e32 v237, s42, v0
	v_add_u32_e32 v238, s44, v0
	v_add_u32_e32 v239, s46, v0
	v_add_u32_e32 v240, s48, v0
	v_add_u32_e32 v241, s51, v0
	v_add_u32_e32 v1, 0x3000, v0
	v_add_u32_e32 v9, 0xfff98000, v1
	v_and_b32_e32 v10, 0x200, v180
	v_cmp_eq_u32_e32 vcc, v9, v194
	s_nop 1
	v_cndmask_b32_e32 v12, 0, v10, vcc
	v_sub_u32_e32 v194, v194, v12
	v_cmp_eq_u32_e32 vcc, v9, v195
	s_nop 1
	v_cndmask_b32_e32 v12, 0, v10, vcc
	v_sub_u32_e32 v195, v195, v12
	v_cmp_eq_u32_e32 vcc, v9, v196
	s_nop 1
	v_cndmask_b32_e32 v12, 0, v10, vcc
	v_sub_u32_e32 v196, v196, v12
	v_cmp_eq_u32_e32 vcc, v9, v197
	s_nop 1
	v_cndmask_b32_e32 v12, 0, v10, vcc
	v_sub_u32_e32 v197, v197, v12
	v_cmp_eq_u32_e32 vcc, v9, v198
	s_nop 1
	v_cndmask_b32_e32 v12, 0, v10, vcc
	v_sub_u32_e32 v198, v198, v12
	v_cmp_eq_u32_e32 vcc, v9, v199
	s_nop 1
	v_cndmask_b32_e32 v12, 0, v10, vcc
	v_sub_u32_e32 v199, v199, v12
	v_cmp_eq_u32_e32 vcc, v9, v200
	s_nop 1
	v_cndmask_b32_e32 v12, 0, v10, vcc
	v_sub_u32_e32 v200, v200, v12
	v_cmp_eq_u32_e32 vcc, v9, v201
	s_nop 1
	v_cndmask_b32_e32 v12, 0, v10, vcc
	v_sub_u32_e32 v201, v201, v12
	v_cmp_eq_u32_e32 vcc, v9, v202
	s_nop 1
	v_cndmask_b32_e32 v12, 0, v10, vcc
	v_sub_u32_e32 v202, v202, v12
	v_cmp_eq_u32_e32 vcc, v9, v203
	s_nop 1
	v_cndmask_b32_e32 v12, 0, v10, vcc
	v_sub_u32_e32 v203, v203, v12
	v_cmp_eq_u32_e32 vcc, v9, v204
	s_nop 1
	v_cndmask_b32_e32 v12, 0, v10, vcc
	v_sub_u32_e32 v204, v204, v12
	v_cmp_eq_u32_e32 vcc, v9, v205
	s_nop 1
	v_cndmask_b32_e32 v12, 0, v10, vcc
	v_sub_u32_e32 v205, v205, v12
	v_cmp_eq_u32_e32 vcc, v9, v206
	s_nop 1
	v_cndmask_b32_e32 v12, 0, v10, vcc
	v_sub_u32_e32 v206, v206, v12
	v_cmp_eq_u32_e32 vcc, v1, v229
	s_nop 1
	v_cndmask_b32_e32 v12, 0, v10, vcc
	v_sub_u32_e32 v229, v229, v12
	v_cmp_eq_u32_e32 vcc, v1, v230
	s_nop 1
	v_cndmask_b32_e32 v12, 0, v10, vcc
	v_sub_u32_e32 v230, v230, v12
	v_cmp_eq_u32_e32 vcc, v1, v231
	s_nop 1
	v_cndmask_b32_e32 v12, 0, v10, vcc
	v_sub_u32_e32 v231, v231, v12
	v_cmp_eq_u32_e32 vcc, v1, v232
	s_nop 1
	v_cndmask_b32_e32 v12, 0, v10, vcc
	v_sub_u32_e32 v232, v232, v12
	v_cmp_eq_u32_e32 vcc, v1, v233
	s_nop 1
	v_cndmask_b32_e32 v12, 0, v10, vcc
	v_sub_u32_e32 v233, v233, v12
	v_cmp_eq_u32_e32 vcc, v1, v234
	s_nop 1
	v_cndmask_b32_e32 v12, 0, v10, vcc
	v_sub_u32_e32 v234, v234, v12
	v_cmp_eq_u32_e32 vcc, v1, v235
	s_nop 1
	v_cndmask_b32_e32 v12, 0, v10, vcc
	v_sub_u32_e32 v235, v235, v12
	v_cmp_eq_u32_e32 vcc, v1, v236
	s_nop 1
	v_cndmask_b32_e32 v12, 0, v10, vcc
	v_sub_u32_e32 v236, v236, v12
	v_cmp_eq_u32_e32 vcc, v1, v237
	s_nop 1
	v_cndmask_b32_e32 v12, 0, v10, vcc
	v_sub_u32_e32 v237, v237, v12
	v_cmp_eq_u32_e32 vcc, v1, v238
	s_nop 1
	v_cndmask_b32_e32 v12, 0, v10, vcc
	v_sub_u32_e32 v238, v238, v12
	v_cmp_eq_u32_e32 vcc, v1, v239
	s_nop 1
	v_cndmask_b32_e32 v12, 0, v10, vcc
	v_sub_u32_e32 v239, v239, v12
	v_cmp_eq_u32_e32 vcc, v1, v240
	s_nop 1
	v_cndmask_b32_e32 v12, 0, v10, vcc
	v_sub_u32_e32 v240, v240, v12
	v_cmp_eq_u32_e32 vcc, v1, v241
	s_nop 1
	v_cndmask_b32_e32 v12, 0, v10, vcc
	v_sub_u32_e32 v241, v241, v12
	v_mad_u32_u24 v0, v8, 13, s37
	v_mov_b32_e32 v1, v59
	v_lshlrev_b64 v[0:1], 10, v[0:1]
	v_lshl_add_u64 v[0:1], s[16:17], 0, v[0:1]
	v_mov_b32_e32 v111, v59
	v_lshl_add_u64 v[0:1], v[0:1], 0, v[58:59]
	v_mul_u32_u24_e32 v61, 0x320, v183
	v_lshlrev_b32_e32 v9, 1, v113
	v_lshlrev_b32_e32 v10, 1, v181
	v_lshlrev_b32_e32 v225, 2, v181
	v_lshl_add_u64 v[176:177], s[14:15], 0, v[110:111]
	v_mul_u32_u24_e32 v111, 0x220, v183
	v_lshl_add_u64 v[178:179], v[0:1], 0, v[6:7]
	v_mul_u32_u24_e32 v0, 0x320, v181
	s_movk_i32 s52, 0x320
	v_add3_u32 v221, v61, v9, v10
	v_lshlrev_b32_e32 v224, 8, v181
	v_sub_u32_e32 v3, v110, v2
	v_mul_u32_u24_e32 v12, 0x220, v181
	v_add3_u32 v9, v111, v9, v10
	s_mov_b32 s14, 0xf010
	v_lshl_add_u32 v1, v113, 2, v225
	v_add_u32_e32 v245, v2, v0
	v_mbcnt_lo_u32_b32 v0, -1, 0
	v_add_u32_e32 v189, 0x27010, v60
	v_cmp_lt_u32_e64 s[4:5], 15, v244
	v_cmp_gt_u32_e64 s[6:7], 16, v244
	v_and_b32_e32 v207, 48, v244
	v_or_b32_e32 v208, s18, v180
	v_lshl_or_b32 v214, s39, 4, v180
	v_lshl_or_b32 v215, s41, 4, v180
	v_lshl_or_b32 v216, s43, 4, v180
	v_lshl_or_b32 v217, s45, 4, v180
	v_lshl_or_b32 v218, s47, 4, v180
	v_lshl_or_b32 v219, s49, 4, v180
	v_lshl_or_b32 v220, s8, 4, v180
	v_cmp_gt_u32_e64 s[8:9], 48, v244
	v_or_b32_e32 v226, 0x100, v224
	v_or_b32_e32 v227, 0x200, v224
	v_or_b32_e32 v228, 0x300, v224
	v_or_b32_e32 v242, v224, v110
	v_add3_u32 v58, v180, v182, s14
	v_mad_u32_u24 v243, v181, s52, v2
	v_accvgpr_write_b32 a136, v183
	v_cmp_eq_u32_e64 s[14:15], 0, v183
	v_accvgpr_write_b32 a240, v1
	v_mov_b32_e32 v113, v112
	v_mbcnt_hi_u32_b32 v246, -1, v0
	v_add_u32_e32 v247, v3, v12
	v_add_u32_e32 v248, 0x3000, v9
	s_mov_b32 s25, 0
	s_mov_b32 s64, 0x40004000
	s_mov_b32 s65, 0
	s_mov_b32 s71, 0
	s_mov_b32 s40, 0
	s_branch .LBB1_75
